# v9
# speedup vs baseline: 1.0021x; 1.0021x over previous
_Z9nerf_mainPKfS0_S0_PKiS2_PKcS0_Pf:
	s_load_dwordx8 s[8:15], s[0:1], 0x20
	s_load_dwordx8 s[24:31], s[0:1], 0x0
	v_readfirstlane_b32 s3, v0
	v_and_b32_e32 v120, 63, v0
	v_lshlrev_b32_e32 v121, 4, v120
	s_mov_b32 s39, 0x20000
	s_waitcnt lgkmcnt(0)
	s_load_dword s50, s[30:31], 0x0
	s_load_dword s51, s[8:9], 0x0
	s_load_dwordx8 s[52:59], s[28:29], 0x0
	s_load_dwordx4 s[60:63], s[28:29], 0x20
	s_lshr_b32 s64, s3, 7
	s_lshl_b32 s65, s2, 2
	s_add_i32 s64, s64, s65
	s_ashr_i32 s65, s64, 31
	s_lshl_b64 s[64:65], s[64:65], 2
	s_add_u32 s66, s24, s64
	s_addc_u32 s67, s25, s65
	s_add_u32 s64, s26, s64
	s_addc_u32 s65, s27, s65
	s_load_dword s68, s[66:67], 0x0
	s_load_dword s69, s[64:65], 0x0
	v_lshlrev_b32_e32 v188, 2, v0
	v_add_u32_e32 v189, 0x1000, v188
	global_load_dword v184, v188, s[12:13]
	global_load_dword v185, v188, s[12:13] offset:2048
	global_load_dword v186, v189, s[12:13]
	global_load_dword v187, v189, s[12:13] offset:2048
	s_and_b32 s37, s11, 0xffff
	s_lshl_b32 s11, s3, 4
	s_mov_b32 s38, 0xf0000
	s_and_b32 s42, s11, 0xfffffc00
	s_mov_b32 s4, s10
	s_mov_b32 s5, s37
	s_mov_b32 s6, s38
	s_mov_b32 s7, s39
	v_or_b32_e32 v125, s42, v121
	s_add_i32 m0, s42, 0x1a000
	s_movk_i32 s11, 0x2000
	buffer_load_dwordx4 v125, s[4:7], 0 offen lds
	s_add_i32 m0, s42, 0x1c000
	s_nop 0
	buffer_load_dwordx4 v125, s[4:7], s11 offen lds
	s_add_i32 m0, s42, 0x1e000
	s_movk_i32 s11, 0x4000
	buffer_load_dwordx4 v125, s[4:7], s11 offen lds
	s_add_i32 m0, s42, 0x20000
	s_movk_i32 s11, 0x6000
	buffer_load_dwordx4 v125, s[4:7], s11 offen lds
	s_add_i32 m0, s42, 0x22000
	s_mov_b32 s11, 0xe8000
	buffer_load_dwordx4 v125, s[4:7], s11 offen lds
	s_mov_b32 s36, s10
	s_waitcnt lgkmcnt(0)
	s_mov_b32 s0, s50
	s_lshl_b32 s1, s2, 2
	s_mov_b32 s2, s51
	s_lshr_b32 s31, s3, 7
	s_bfe_u32 s30, s3, 0x10006
	s_waitcnt lgkmcnt(0)
	v_cvt_f32_i32_e32 v1, s0
	s_add_i32 s12, s31, s1
	s_add_i32 s1, s0, 0xf423f
	s_cmp_lt_u32 s1, 0x1e847f
	v_mov_b32_e32 v2, s0
	s_cselect_b64 vcc, -1, 0
	v_cndmask_b32_e32 v123, v2, v1, vcc
	v_cvt_f32_i32_e32 v1, s2
	s_add_i32 s0, s2, 0xf423f
	s_cmp_lt_u32 s0, 0x1e847f
	v_mov_b32_e32 v2, s2
	s_cselect_b64 vcc, -1, 0
	v_cndmask_b32_e32 v1, v2, v1, vcc
	v_sub_f32_e32 v122, v1, v123
	s_mov_b32 s2, 0x427c0000
	v_div_scale_f32 v1, s[0:1], s2, s2, v122
	v_rcp_f32_e32 v2, v1
	s_ashr_i32 s13, s12, 31
	s_lshl_b64 s[0:1], s[12:13], 2
	s_add_u32 s4, s24, s0
	v_fma_f32 v5, -v1, v2, 1.0
	s_addc_u32 s5, s25, s1
	v_fmac_f32_e32 v2, v5, v2
	v_div_scale_f32 v5, vcc, v122, s2, v122
	s_add_u32 s0, s26, s0
	v_mul_f32_e32 v6, v5, v2
	s_mov_b64 s[16:17], s[52:53]
	s_mov_b64 s[18:19], s[54:55]
	s_mov_b64 s[20:21], s[56:57]
	s_mov_b64 s[22:23], s[58:59]
	s_addc_u32 s1, s27, s1
	v_fma_f32 v7, -v1, v6, v5
	s_mov_b32 s4, s68
	v_fmac_f32_e32 v6, v7, v2
	s_mov_b32 s0, s69
	v_fma_f32 v1, -v1, v6, v5
	v_div_fmas_f32 v1, v1, v2, v6
	v_div_fixup_f32 v124, v1, s2, v122
	s_waitcnt lgkmcnt(0)
	v_mov_b32_e32 v1, s16
	s_mov_b64 s[24:25], s[60:61]
	s_mov_b64 s[26:27], s[62:63]
	v_mul_f32_e32 v1, s4, v1
	v_mov_b32_e32 v2, s0
	v_fma_f32 v1, s17, -v2, v1
	v_add_f32_e32 v127, s19, v1
	v_mov_b32_e32 v1, s20
	v_mul_f32_e32 v1, s4, v1
	v_fma_f32 v1, s21, -v2, v1
	v_add_f32_e32 v128, s23, v1
	s_waitcnt lgkmcnt(0)
	v_mov_b32_e32 v1, s24
	v_mul_f32_e32 v1, s4, v1
	v_and_b32_e32 v3, 15, v0
	v_fma_f32 v1, s25, -v2, v1
	v_and_b32_e32 v131, 48, v0
	v_lshl_or_b32 v0, s30, 6, v120
	v_add_f32_e32 v129, s27, v1
	v_add_u32_e32 v1, 1, v0
	v_cvt_f32_ubyte0_e32 v1, v1
	s_mov_b32 s4, 0x43010000
	s_and_b32 s19, s3, 0xffffff80
	v_div_scale_f32 v2, s[2:3], s4, s4, v1
	v_lshl_or_b32 v130, s30, 5, v3
	v_rcp_f32_e32 v3, v2
	v_lshrrev_b32_e32 v4, 4, v120
	v_cmp_eq_u32_e64 s[8:9], 2, v4
	v_cmp_eq_u32_e64 s[10:11], 1, v4
	v_fma_f32 v5, -v2, v3, 1.0
	v_fmac_f32_e32 v3, v5, v3
	v_div_scale_f32 v5, vcc, v1, s4, v1
	v_mul_f32_e32 v6, v5, v3
	v_fma_f32 v7, -v2, v6, v5
	v_fmac_f32_e32 v6, v7, v3
	v_fma_f32 v2, -v2, v6, v5
	v_div_fmas_f32 v2, v2, v3, v6
	v_div_fixup_f32 v134, v2, s4, v1
	v_add_u32_e32 v2, -1, v4
	v_cmp_gt_u32_e32 vcc, 2, v2
	v_mov_b32_e32 v2, 0x401550d3
	v_mov_b32_e32 v3, 0x436d0620
	v_cndmask_b32_e64 v5, v2, v3, s[8:9]
	v_mov_b32_e32 v6, 0x412e2e5e
	v_cmp_eq_u32_e64 s[0:1], 3, v4
	v_cndmask_b32_e64 v4, v5, v6, s[10:11]
	v_cmp_gt_u32_e64 s[2:3], 16, v120
	v_bfrev_b32_e32 v5, 34
	v_mov_b32_e32 v8, 0x41bc2043
	v_cndmask_b32_e64 v140, v4, 0.5, s[2:3]
	v_mov_b32_e32 v4, 0x40a14518
	v_cndmask_b32_e64 v7, v4, v5, s[8:9]
	v_cndmask_b32_e64 v7, v7, v8, s[10:11]
	v_mov_b32_e32 v9, 0x3f8a3f66
	v_cndmask_b32_e64 v141, v7, v9, s[2:3]
	v_cndmask_b32_e64 v7, v6, 0.5, s[8:9]
	v_cndmask_b32_e64 v6, v3, v6, s[8:9]
	v_mov_b32_e32 v10, 0x424b2ff5
	v_cndmask_b32_e64 v6, v6, 0.5, s[10:11]
	v_cndmask_b32_e64 v144, v6, v10, s[2:3]
	v_cndmask_b32_e64 v6, v5, v8, s[8:9]
	v_or_b32_e32 v0, s19, v0
	v_mov_b32_e32 v11, 0x42db7457
	v_cndmask_b32_e64 v6, v6, v9, s[10:11]
	v_lshlrev_b32_e32 v0, 2, v0
	v_cndmask_b32_e64 v7, v7, v10, s[10:11]
	v_cndmask_b32_e64 v145, v6, v11, s[2:3]
	v_cndmask_b32_e64 v6, 0, v10, s[8:9]
	v_add_u32_e32 v135, 0x15000, v0
	v_add_u32_e32 v136, 0x15800, v0
	v_cvt_f32_ubyte0_e32 v0, v130
	v_or_b32_e32 v138, 16, v130
	v_cndmask_b32_e64 v142, v7, v2, s[2:3]
	v_cndmask_b32_e64 v2, v6, v2, s[10:11]
	s_lshl_b32 s13, s31, 10
	s_lshl_b32 s44, s31, 8
	v_fma_f32 v137, v0, v124, v123
	v_cvt_f32_ubyte0_e32 v0, v138
	v_cndmask_b32_e64 v7, v8, v9, s[8:9]
	v_cndmask_b32_e64 v146, v2, v3, s[2:3]
	v_cndmask_b32_e64 v2, 0, v11, s[8:9]
	s_lshl_b32 s27, s19, 2
	s_add_i32 s13, s13, 0x12000
	s_add_i32 s44, s44, 0x16000
	v_fma_f32 v139, v0, v124, v123
	v_lshlrev_b32_e32 v0, 4, v130
	v_lshlrev_b32_e32 v1, 4, v138
	v_cndmask_b32_e64 v7, v7, v11, s[10:11]
	v_cndmask_b32_e64 v2, v2, v4, s[10:11]
	v_or_b32_e32 v126, 0x2000, v121
	s_add_i32 s23, s27, 0x15000
	s_add_i32 s28, s42, 0xa000
	s_add_i32 s29, s42, 0xc000
	s_add_i32 s33, s42, 0xe000
	s_add_i32 s34, s42, 0x10000
	s_add_i32 s35, s42, 0x2000
	s_add_i32 s40, s42, 0x8000
	s_add_i32 s41, s42, 0x6000
	s_addk_i32 s42, 0x4000
	s_sub_i32 s43, s19, 64
	v_lshl_or_b32 v132, v120, 4, s13
	v_lshl_or_b32 v133, v120, 2, s44
	s_mov_b32 s20, 1
	s_or_b64 s[4:5], s[2:3], vcc
	s_or_b64 s[6:7], s[2:3], s[10:11]
	v_cndmask_b32_e64 v143, v7, v4, s[2:3]
	s_mov_b32 s45, 0
	v_cndmask_b32_e64 v147, v2, v5, s[2:3]
	v_or_b32_e32 v148, 0x1a000, v121
	v_or_b32_e32 v149, 0x1a400, v121
	v_or_b32_e32 v150, 0x1a800, v121
	v_or_b32_e32 v151, 0x1ac00, v121
	v_or_b32_e32 v152, 0x1b000, v121
	v_or_b32_e32 v153, 0x1b400, v121
	v_or_b32_e32 v154, 0x1b800, v121
	v_or_b32_e32 v155, 0x1bc00, v121
	v_or_b32_e32 v156, 0x1c000, v121
	v_or_b32_e32 v157, 0x1c400, v121
	v_or_b32_e32 v158, 0x1c800, v121
	v_or_b32_e32 v159, 0x1cc00, v121
	v_or_b32_e32 v160, 0x1d000, v121
	v_or_b32_e32 v161, 0x1d400, v121
	v_or_b32_e32 v162, 0x1d800, v121
	v_or_b32_e32 v163, 0x1dc00, v121
	v_or_b32_e32 v164, 0x1e000, v121
	v_or_b32_e32 v165, 0x1e400, v121
	v_or_b32_e32 v166, 0x1e800, v121
	v_or_b32_e32 v167, 0x1ec00, v121
	v_or_b32_e32 v168, 0x1f000, v121
	v_or_b32_e32 v169, 0x1f400, v121
	v_or_b32_e32 v170, 0x1f800, v121
	v_or_b32_e32 v171, 0x1fc00, v121
	v_or_b32_e32 v172, 0x20000, v121
	v_or_b32_e32 v173, 0x20400, v121
	v_or_b32_e32 v174, 0x20800, v121
	v_or_b32_e32 v175, 0x20c00, v121
	v_or_b32_e32 v176, 0x21000, v121
	v_or_b32_e32 v177, 0x21400, v121
	v_or_b32_e32 v178, 0x21800, v121
	v_or_b32_e32 v179, 0x21c00, v121
	v_add_u32_e32 v180, s13, v0
	v_add_u32_e32 v181, s13, v1
	v_mov_b32_e32 v182, 0x13000
	s_waitcnt vmcnt(5)
	ds_write_b32 v188, v184
	ds_write_b32 v188, v185 offset:2048
	ds_write_b32 v188, v186 offset:4096
	ds_write_b32 v188, v187 offset:6144
	s_branch .LBB1_5

.LBB1_20:
	s_or_b64 exec, exec, s[20:21]
	s_andn2_b64 vcc, exec, s[10:11]
	s_cbranch_vccnz .LBB1_4
	s_waitcnt lgkmcnt(0)
	s_barrier
	s_nop 0
	ds_read_b128 v[0:3], v132
	s_waitcnt lgkmcnt(0)
	v_mov_b32_e32 v1, 0
	v_add_f32_dpp v0, v0, v0 row_shr:1 row_mask:0xf bank_mask:0xf bound_ctrl:1
	s_nop 1
	v_add_f32_dpp v0, v0, v0 row_shr:2 row_mask:0xf bank_mask:0xf bound_ctrl:1
	s_nop 1
	v_add_f32_dpp v0, v0, v0 row_shr:4 row_mask:0xf bank_mask:0xf bound_ctrl:1
	s_nop 1
	v_add_f32_dpp v0, v0, v0 row_shr:8 row_mask:0xf bank_mask:0xf bound_ctrl:1
	s_nop 1
	v_mov_b32_dpp v1, v0 row_bcast:15 row_mask:0xa bank_mask:0xf
	v_add_f32_e32 v0, v0, v1
	v_mov_b32_e32 v1, 0
	s_nop 1
	v_mov_b32_dpp v1, v0 row_bcast:31 row_mask:0xc bank_mask:0xf
	v_add_f32_e32 v0, v0, v1
	v_mov_b32_e32 v1, s44
	ds_write_b32 v133, v0
	s_waitcnt lgkmcnt(0)
	s_barrier
	v_readlane_b32 s8, v0, 0
	v_readlane_b32 s9, v0, 63
	v_readlane_b32 s10, v0, 15
	v_readlane_b32 s11, v0, 31
	v_readlane_b32 s16, v0, 47
	s_nop 0
	v_mov_b32_e32 v0, s8
	v_sub_f32_e32 v0, s9, v0
	v_fma_f32 v0, v134, v0, s8
	v_mov_b32_e32 v1, 0
	v_sub_f32_e32 v10, s10, v0
	v_lshrrev_b32_e32 v10, 31, v10
	v_add_u32_e32 v1, v1, v10
	v_sub_f32_e32 v10, s11, v0
	v_lshrrev_b32_e32 v10, 31, v10
	v_add_u32_e32 v1, v1, v10
	v_sub_f32_e32 v10, s16, v0
	v_lshrrev_b32_e32 v10, 31, v10
	v_add_u32_e32 v1, v1, v10
	v_sub_f32_e32 v10, s9, v0
	v_lshrrev_b32_e32 v10, 31, v10
	v_add_u32_e32 v1, v1, v10
	v_min_u32_e32 v1, 3, v1
	v_lshl_add_u32 v10, v1, 6, s44
	ds_read_b128 v[12:15], v10
	ds_read_b128 v[16:19], v10 offset:16
	ds_read_b128 v[20:23], v10 offset:32
	ds_read_b128 v[24:27], v10 offset:48
	v_lshlrev_b32_e32 v3, 4, v1
	s_waitcnt lgkmcnt(0)
	v_sub_f32_e32 v10, v12, v0
	v_lshrrev_b32_e32 v10, 31, v10
	v_add_u32_e32 v3, v3, v10
	v_sub_f32_e32 v10, v13, v0
	v_lshrrev_b32_e32 v10, 31, v10
	v_add_u32_e32 v3, v3, v10
	v_sub_f32_e32 v10, v14, v0
	v_lshrrev_b32_e32 v10, 31, v10
	v_add_u32_e32 v3, v3, v10
	v_sub_f32_e32 v10, v15, v0
	v_lshrrev_b32_e32 v10, 31, v10
	v_add_u32_e32 v3, v3, v10
	v_sub_f32_e32 v10, v16, v0
	v_lshrrev_b32_e32 v10, 31, v10
	v_add_u32_e32 v3, v3, v10
	v_sub_f32_e32 v10, v17, v0
	v_lshrrev_b32_e32 v10, 31, v10
	v_add_u32_e32 v3, v3, v10
	v_sub_f32_e32 v10, v18, v0
	v_lshrrev_b32_e32 v10, 31, v10
	v_add_u32_e32 v3, v3, v10
	v_sub_f32_e32 v10, v19, v0
	v_lshrrev_b32_e32 v10, 31, v10
	v_add_u32_e32 v3, v3, v10
	v_sub_f32_e32 v10, v20, v0
	v_lshrrev_b32_e32 v10, 31, v10
	v_add_u32_e32 v3, v3, v10
	v_sub_f32_e32 v10, v21, v0
	v_lshrrev_b32_e32 v10, 31, v10
	v_add_u32_e32 v3, v3, v10
	v_sub_f32_e32 v10, v22, v0
	v_lshrrev_b32_e32 v10, 31, v10
	v_add_u32_e32 v3, v3, v10
	v_sub_f32_e32 v10, v23, v0
	v_lshrrev_b32_e32 v10, 31, v10
	v_add_u32_e32 v3, v3, v10
	v_sub_f32_e32 v10, v24, v0
	v_lshrrev_b32_e32 v10, 31, v10
	v_add_u32_e32 v3, v3, v10
	v_sub_f32_e32 v10, v25, v0
	v_lshrrev_b32_e32 v10, 31, v10
	v_add_u32_e32 v3, v3, v10
	v_sub_f32_e32 v10, v26, v0
	v_lshrrev_b32_e32 v10, 31, v10
	v_add_u32_e32 v3, v3, v10
	v_sub_f32_e32 v10, v27, v0
	v_lshrrev_b32_e32 v10, 31, v10
	v_add_u32_e32 v3, v3, v10
	v_med3_u32 v4, v3, 1, 64
	v_add_u32_e32 v1, -1, v4
	v_lshl_add_u32 v2, v1, 2, s44
	ds_read_b32 v2, v2
	v_cmp_gt_u32_e32 vcc, 64, v3
	v_mov_b32_e32 v3, 0
	s_and_saveexec_b64 s[8:9], vcc
	s_cbranch_execz .LBB1_3
	v_lshl_add_u32 v3, v4, 4, s13
	ds_read_b128 v[4:7], v3
	s_waitcnt lgkmcnt(0)
	v_div_scale_f32 v3, s[10:11], v4, v4, v124
	v_rcp_f32_e32 v5, v3
	v_div_scale_f32 v6, vcc, v124, v4, v124
	v_fma_f32 v7, -v3, v5, 1.0
	v_fmac_f32_e32 v5, v7, v5
	v_mul_f32_e32 v7, v6, v5
	v_fma_f32 v8, -v3, v7, v6
	v_fmac_f32_e32 v7, v8, v5
	v_fma_f32 v3, -v3, v7, v6
	v_div_fmas_f32 v3, v3, v5, v7
	v_div_fixup_f32 v3, v3, v4, v124
	s_branch .LBB1_3
